# P2: odd workgroups run the indexer scores / top-k selection before the pool / conv pass, even ones after (on top of the hand-written pool / conv pass and late conversion)
# speedup vs baseline: 1.0112x; 1.0024x over previous
;     __device__ __forceinline__ const char* pb(const Unit& u) const { return (const char*)(Bt + ((size_t)u.pn * BM * ldb + (size_t)u.sub * b_sub)); }
; __device__ __forceinline__ unsigned pk2(float lo, float hi) { return pg8::cvt_pk_bf16(lo, hi); }
; __device__ __forceinline__ void unpack8(const v4u w, float (&f)[8]) { f[0] = bflo(w.x); f[1] = bfhi(w.x); f[2] = bflo(w.y); f[3] = bfhi(w.y); f[4] = bflo(w.z); f[5] = bfhi(w.z); f[6] = bflo(w.w); f[7] = bfhi(w.w); }
; __device__ __forceinline__ int lane_id() { int l; asm volatile("s_nop 4\n\tv_mbcnt_lo_u32_b32 %0, -1, 0\n\tv_mbcnt_hi_u32_b32 %0, -1, %0\n\ts_nop 4" : "=v"(l)); return l; }
; template <int W> __device__ __forceinline__ void pool_item(Frame& F, int row, int t, int c8) {
;     float s[8], u[8];
; #pragma unroll
;     for (int i = 0; i < 8; ++i) s[i] = 0.f;
;     v4u ld[W];
; #pragma unroll
;     for (int k = 0; k < W; ++k) { const int kk = (t - k) >= 0 ? k : t; ld[k] = *(const v4u*)(F.PROJ + (size_t)(row - kk) * INWP + O_UPOOL + c8); }
; #pragma unroll
;     for (int k = W - 1; k >= 0; --k) { unpack8(ld[k], u); const float wgt = (t - k) >= 0 ? 1.f : 0.f;
; #pragma unroll
;         for (int i = 0; i < 8; ++i) s[i] += wgt * u[i]; }
;     const int cnt = (t + 1) < W ? (t + 1) : W;
;     const float inv = 1.0f / (float)cnt;
;     v4u o; o.x = pk2(s[0] * inv - u[0], s[1] * inv - u[1]); o.y = pk2(s[2] * inv - u[2], s[3] * inv - u[3]); o.z = pk2(s[4] * inv - u[4], s[5] * inv - u[5]); o.w = pk2(s[6] * inv - u[6], s[7] * inv - u[7]);
;     *(v4u*)(F.Y + (size_t)row * 1024 + c8) = o;
; }
; __device__ __forceinline__ void poolconv_phase(Frame& F, const float* conv_w_l) {
;     int tid = F.wave * 64 + lane_id(); asm volatile("" : "+v"(tid));
;     const int gt = F.vcu * NTHR + tid, NGT = F.G * NTHR;
;     for (int idx = gt; idx < M * 128; idx += NGT) {
;         const int grp = idx / (M * 32), rem = idx - grp * (M * 32), row = rem >> 5, c8 = grp * 256 + (rem & 31) * 8, t = row & (SEQ - 1);
;         if (grp == 0) pool_item<2>(F, row, t, c8); else if (grp == 1) pool_item<4>(F, row, t, c8); else if (grp == 2) pool_item<8>(F, row, t, c8); else pool_item<16>(F, row, t, c8);
; __global__ void __launch_bounds__(NTHR, 2) mk_fwd(Args args) {
;     ...
;         if (IN(pb + 1)) { poolconv_phase(F, F.conv_w + (size_t)l * 3 * 1024); scores_phase_mfma(F); GRID_BAR(); }
.LBB0_239:
	v_readlane_b32 s0, v255, 42
	s_add_i32 s4, s0, 2
	v_readlane_b32 s0, v251, 14
	v_readlane_b32 s1, v251, 15
	s_cmp_le_i32 s0, s4
	s_cselect_b64 s[2:3], -1, 0
	s_cmp_lt_i32 s4, s1
	s_cselect_b64 s[4:5], -1, 0
	s_mov_b32 s1, s63
	s_and_b64 s[2:3], s[2:3], s[4:5]
	v_writelane_b32 v255, s0, 45
	s_andn2_b64 vcc, exec, s[2:3]
	s_nop 0
	v_writelane_b32 v255, s1, 46
	s_cbranch_vccnz .LBB0_540
	v_readlane_b32 s0, v255, 12
	s_mov_b32 s100, 0
	s_nop 0
	s_bitcmp1_b32 s0, 0
	s_cbranch_scc0 .Lp2_pool_start
	s_mov_b32 s100, 1
	s_mov_b64 s[2:3], -1
	s_branch .LBB0_261
.Lp2_pool_start:
	v_mbcnt_lo_u32_b32 v0, -1, 0
	v_mbcnt_hi_u32_b32 v0, -1, v0
	v_readlane_b32 s0, v255, 12
	v_readlane_b32 s14, v251, 40
	v_readlane_b32 s15, v251, 41
	v_readlane_b32 s10, v255, 43
	s_and_b32 s1, s0, 7
	s_lshl_b32 s1, s1, 5
	s_lshr_b32 s0, s0, 3
	s_or_b32 s1, s1, s0
	s_lshl_b32 s2, s1, 9
	s_lshl_b32 s3, s35, 6
	s_add_i32 s2, s2, s3
	v_add_u32_e32 v1, s2, v0
	s_lshr_b32 s3, s1, 7
	v_and_b32_e32 v2, 0xffff, v1
	v_lshrrev_b32_e32 v2, 5, v2
	v_and_b32_e32 v3, 31, v1
	v_lshlrev_b32_e32 v4, 2, v2
	v_and_b32_e32 v5, 0x7ff, v4
	v_mul_u32_u24_e32 v6, 0x3600, v5
	v_mul_u32_u24_e32 v7, 0x3600, v4
	v_lshlrev_b32_e32 v8, 4, v3
	v_lshl_add_u32 v9, v4, 11, v8
	v_add_u32_e32 v7, v7, v8
	s_cmp_eq_u32 s3, 0
	s_cbranch_scc0 .Lpc_g1
	v_add_u32_e32 v14, 0x0, v7
	v_add_u32_e32 v15, 0x600, v7
	v_add_u32_e32 v16, 0x0, v9
	v_add_u32_e32 v17, 0x600, v9
	v_min_u32_e32 v11, 0x3600, v6
	v_sub_u32_e32 v12, v14, v11
	global_load_dwordx4 v[20:23], v12, s[96:97]
	global_load_dwordx4 v[24:27], v14, s[96:97]
	v_add_u32_e32 v12, 0x3600, v14
	global_load_dwordx4 v[28:31], v12, s[96:97]
	v_add_u32_e32 v12, 0x6c00, v14
	global_load_dwordx4 v[32:35], v12, s[96:97]
	v_add_u32_e32 v12, 0xa200, v14
	global_load_dwordx4 v[36:39], v12, s[96:97]
	v_min_u32_e32 v11, 0x32a00, v6
	v_sub_u32_e32 v12, v15, v11
	global_load_dwordx4 v[48:51], v12, s[96:97]
	v_min_u32_e32 v11, 0x2f400, v6
	v_sub_u32_e32 v12, v15, v11
	global_load_dwordx4 v[52:55], v12, s[96:97]
	v_min_u32_e32 v11, 0x2be00, v6
	v_sub_u32_e32 v12, v15, v11
	global_load_dwordx4 v[56:59], v12, s[96:97]
	v_min_u32_e32 v11, 0x28800, v6
	v_sub_u32_e32 v12, v15, v11
	global_load_dwordx4 v[60:63], v12, s[96:97]
	v_min_u32_e32 v11, 0x25200, v6
	v_sub_u32_e32 v12, v15, v11
	global_load_dwordx4 v[64:67], v12, s[96:97]
	v_min_u32_e32 v11, 0x21c00, v6
	v_sub_u32_e32 v12, v15, v11
	global_load_dwordx4 v[68:71], v12, s[96:97]
	v_min_u32_e32 v11, 0x1e600, v6
	v_sub_u32_e32 v12, v15, v11
	global_load_dwordx4 v[72:75], v12, s[96:97]
	v_min_u32_e32 v11, 0x1b000, v6
	v_sub_u32_e32 v12, v15, v11
	global_load_dwordx4 v[76:79], v12, s[96:97]
	v_min_u32_e32 v11, 0x17a00, v6
	v_sub_u32_e32 v12, v15, v11
	global_load_dwordx4 v[80:83], v12, s[96:97]
	v_min_u32_e32 v11, 0x14400, v6
	v_sub_u32_e32 v12, v15, v11
	global_load_dwordx4 v[84:87], v12, s[96:97]
	v_min_u32_e32 v11, 0x10e00, v6
	v_sub_u32_e32 v12, v15, v11
	global_load_dwordx4 v[88:91], v12, s[96:97]
	v_min_u32_e32 v11, 0xd800, v6
	v_sub_u32_e32 v12, v15, v11
	global_load_dwordx4 v[92:95], v12, s[96:97]
	v_min_u32_e32 v11, 0xa200, v6
	v_sub_u32_e32 v12, v15, v11
	global_load_dwordx4 v[96:99], v12, s[96:97]
	v_min_u32_e32 v11, 0x6c00, v6
	v_sub_u32_e32 v12, v15, v11
	global_load_dwordx4 v[100:103], v12, s[96:97]
	v_min_u32_e32 v11, 0x3600, v6
	v_sub_u32_e32 v12, v15, v11
	global_load_dwordx4 v[104:107], v12, s[96:97]
	global_load_dwordx4 v[108:111], v15, s[96:97]
	v_add_u32_e32 v12, 0x3600, v15
	global_load_dwordx4 v[112:115], v12, s[96:97]
	v_add_u32_e32 v12, 0x6c00, v15
	global_load_dwordx4 v[116:119], v12, s[96:97]
	v_add_u32_e32 v12, 0xa200, v15
	global_load_dwordx4 v[120:123], v12, s[96:97]
	s_waitcnt vmcnt(19)
	v_cmp_le_u32_e32 vcc, 1, v5
	s_nop 1
	v_cndmask_b32_e32 v20, 0, v20, vcc
	v_cndmask_b32_e32 v21, 0, v21, vcc
	v_cndmask_b32_e32 v22, 0, v22, vcc
	v_cndmask_b32_e32 v23, 0, v23, vcc
	v_add_u32_e32 v226, 1, v5
	v_min_u32_e32 v226, 2, v226
	v_cvt_f32_u32_e32 v226, v226
	v_rcp_f32_e32 v226, v226
	v_add_u32_e32 v227, 2, v5
	v_min_u32_e32 v227, 2, v227
	v_cvt_f32_u32_e32 v227, v227
	v_rcp_f32_e32 v227, v227
	v_add_u32_e32 v228, 3, v5
	v_min_u32_e32 v228, 2, v228
	v_cvt_f32_u32_e32 v228, v228
	v_rcp_f32_e32 v228, v228
	v_add_u32_e32 v229, 4, v5
	v_min_u32_e32 v229, 2, v229
	v_cvt_f32_u32_e32 v229, v229
	v_rcp_f32_e32 v229, v229
	v_lshlrev_b32_e32 v124, 16, v20
	v_and_b32_e32 v125, 0xffff0000, v20
	v_lshlrev_b32_e32 v126, 16, v24
	v_and_b32_e32 v127, 0xffff0000, v24
	v_lshlrev_b32_e32 v128, 16, v28
	v_and_b32_e32 v129, 0xffff0000, v28
	v_lshlrev_b32_e32 v130, 16, v32
	v_and_b32_e32 v131, 0xffff0000, v32
	v_lshlrev_b32_e32 v132, 16, v36
	v_and_b32_e32 v133, 0xffff0000, v36
	v_add_f32_e32 v194, v124, v126
	v_fma_f32 v194, v194, v226, -v126
	v_add_f32_e32 v195, v125, v127
	v_fma_f32 v195, v195, v226, -v127
	v_add_f32_e32 v202, v126, v128
	v_fma_f32 v202, v202, v227, -v128
	v_add_f32_e32 v203, v127, v129
	v_fma_f32 v203, v203, v227, -v129
	v_add_f32_e32 v210, v128, v130
	v_fma_f32 v210, v210, v228, -v130
	v_add_f32_e32 v211, v129, v131
	v_fma_f32 v211, v211, v228, -v131
	v_add_f32_e32 v218, v130, v132
	v_fma_f32 v218, v218, v229, -v132
	v_add_f32_e32 v219, v131, v133
	v_fma_f32 v219, v219, v229, -v133
	v_lshlrev_b32_e32 v124, 16, v21
	v_and_b32_e32 v125, 0xffff0000, v21
	v_lshlrev_b32_e32 v126, 16, v25
	v_and_b32_e32 v127, 0xffff0000, v25
	v_lshlrev_b32_e32 v128, 16, v29
	v_and_b32_e32 v129, 0xffff0000, v29
	v_lshlrev_b32_e32 v130, 16, v33
	v_and_b32_e32 v131, 0xffff0000, v33
	v_lshlrev_b32_e32 v132, 16, v37
	v_and_b32_e32 v133, 0xffff0000, v37
	v_add_f32_e32 v196, v124, v126
	v_fma_f32 v196, v196, v226, -v126
; __device__ __forceinline__ unsigned pk2(float lo, float hi) { return pg8::cvt_pk_bf16(lo, hi); }
; __device__ __forceinline__ void unpack8(const v4u w, float (&f)[8]) { f[0] = bflo(w.x); f[1] = bfhi(w.x); f[2] = bflo(w.y); f[3] = bfhi(w.y); f[4] = bflo(w.z); f[5] = bfhi(w.z); f[6] = bflo(w.w); f[7] = bfhi(w.w); }
; template <int W> __device__ __forceinline__ void pool_item(Frame& F, int row, int t, int c8) {
;     float s[8], u[8];
; #pragma unroll
;     for (int i = 0; i < 8; ++i) s[i] = 0.f;
;     v4u ld[W];
; #pragma unroll
;     for (int k = 0; k < W; ++k) { const int kk = (t - k) >= 0 ? k : t; ld[k] = *(const v4u*)(F.PROJ + (size_t)(row - kk) * INWP + O_UPOOL + c8); }
; #pragma unroll
;     for (int k = W - 1; k >= 0; --k) { unpack8(ld[k], u); const float wgt = (t - k) >= 0 ? 1.f : 0.f;
; #pragma unroll
;         for (int i = 0; i < 8; ++i) s[i] += wgt * u[i]; }
;     const int cnt = (t + 1) < W ? (t + 1) : W;
;     const float inv = 1.0f / (float)cnt;
;     v4u o; o.x = pk2(s[0] * inv - u[0], s[1] * inv - u[1]); o.y = pk2(s[2] * inv - u[2], s[3] * inv - u[3]); o.z = pk2(s[4] * inv - u[4], s[5] * inv - u[5]); o.w = pk2(s[6] * inv - u[6], s[7] * inv - u[7]);
;     *(v4u*)(F.Y + (size_t)row * 1024 + c8) = o;
; }
	v_add_f32_e32 v197, v125, v127
	v_fma_f32 v197, v197, v226, -v127
	v_add_f32_e32 v204, v126, v128
	v_fma_f32 v204, v204, v227, -v128
	v_add_f32_e32 v205, v127, v129
	v_fma_f32 v205, v205, v227, -v129
	v_add_f32_e32 v212, v128, v130
	v_fma_f32 v212, v212, v228, -v130
	v_add_f32_e32 v213, v129, v131
	v_fma_f32 v213, v213, v228, -v131
	v_add_f32_e32 v220, v130, v132
	v_fma_f32 v220, v220, v229, -v132
	v_add_f32_e32 v221, v131, v133
	v_fma_f32 v221, v221, v229, -v133
	v_lshlrev_b32_e32 v124, 16, v22
	v_and_b32_e32 v125, 0xffff0000, v22
	v_lshlrev_b32_e32 v126, 16, v26
	v_and_b32_e32 v127, 0xffff0000, v26
	v_lshlrev_b32_e32 v128, 16, v30
	v_and_b32_e32 v129, 0xffff0000, v30
	v_lshlrev_b32_e32 v130, 16, v34
	v_and_b32_e32 v131, 0xffff0000, v34
	v_lshlrev_b32_e32 v132, 16, v38
	v_and_b32_e32 v133, 0xffff0000, v38
	v_add_f32_e32 v198, v124, v126
	v_fma_f32 v198, v198, v226, -v126
	v_add_f32_e32 v199, v125, v127
	v_fma_f32 v199, v199, v226, -v127
	v_add_f32_e32 v206, v126, v128
	v_fma_f32 v206, v206, v227, -v128
	v_add_f32_e32 v207, v127, v129
	v_fma_f32 v207, v207, v227, -v129
	v_add_f32_e32 v214, v128, v130
	v_fma_f32 v214, v214, v228, -v130
	v_add_f32_e32 v215, v129, v131
	v_fma_f32 v215, v215, v228, -v131
	v_add_f32_e32 v222, v130, v132
	v_fma_f32 v222, v222, v229, -v132
	v_add_f32_e32 v223, v131, v133
	v_fma_f32 v223, v223, v229, -v133
	v_lshlrev_b32_e32 v124, 16, v23
	v_and_b32_e32 v125, 0xffff0000, v23
	v_lshlrev_b32_e32 v126, 16, v27
	v_and_b32_e32 v127, 0xffff0000, v27
	v_lshlrev_b32_e32 v128, 16, v31
	v_and_b32_e32 v129, 0xffff0000, v31
	v_lshlrev_b32_e32 v130, 16, v35
	v_and_b32_e32 v131, 0xffff0000, v35
	v_lshlrev_b32_e32 v132, 16, v39
	v_and_b32_e32 v133, 0xffff0000, v39
	v_add_f32_e32 v200, v124, v126
	v_fma_f32 v200, v200, v226, -v126
	v_add_f32_e32 v201, v125, v127
	v_fma_f32 v201, v201, v226, -v127
	v_add_f32_e32 v208, v126, v128
	v_fma_f32 v208, v208, v227, -v128
	v_add_f32_e32 v209, v127, v129
	v_fma_f32 v209, v209, v227, -v129
	v_add_f32_e32 v216, v128, v130
	v_fma_f32 v216, v216, v228, -v130
	v_add_f32_e32 v217, v129, v131
	v_fma_f32 v217, v217, v228, -v131
	v_add_f32_e32 v224, v130, v132
	v_fma_f32 v224, v224, v229, -v132
	v_add_f32_e32 v225, v131, v133
	v_fma_f32 v225, v225, v229, -v133
	v_cvt_pk_bf16_f32 v194, v194, v195
	v_cvt_pk_bf16_f32 v195, v196, v197
	v_cvt_pk_bf16_f32 v196, v198, v199
	v_cvt_pk_bf16_f32 v197, v200, v201
	global_store_dwordx4 v16, v[194:197], s[14:15]
	v_cvt_pk_bf16_f32 v202, v202, v203
	v_cvt_pk_bf16_f32 v203, v204, v205
	v_cvt_pk_bf16_f32 v204, v206, v207
	v_cvt_pk_bf16_f32 v205, v208, v209
	v_add_u32_e32 v13, 0x800, v16
	global_store_dwordx4 v13, v[202:205], s[14:15]
	v_cvt_pk_bf16_f32 v210, v210, v211
	v_cvt_pk_bf16_f32 v211, v212, v213
	v_cvt_pk_bf16_f32 v212, v214, v215
	v_cvt_pk_bf16_f32 v213, v216, v217
	v_add_u32_e32 v13, 0x1000, v16
	global_store_dwordx4 v13, v[210:213], s[14:15]
	v_cvt_pk_bf16_f32 v218, v218, v219
	v_cvt_pk_bf16_f32 v219, v220, v221
	v_cvt_pk_bf16_f32 v220, v222, v223
	v_cvt_pk_bf16_f32 v221, v224, v225
	v_add_u32_e32 v13, 0x1800, v16
	global_store_dwordx4 v13, v[218:221], s[14:15]
	s_waitcnt vmcnt(4)
	v_cmp_le_u32_e32 vcc, 15, v5
	s_nop 1
	v_cndmask_b32_e32 v48, 0, v48, vcc
	v_cndmask_b32_e32 v49, 0, v49, vcc
	v_cndmask_b32_e32 v50, 0, v50, vcc
	v_cndmask_b32_e32 v51, 0, v51, vcc
	v_cmp_le_u32_e32 vcc, 14, v5
	s_nop 1
	v_cndmask_b32_e32 v52, 0, v52, vcc
	v_cndmask_b32_e32 v53, 0, v53, vcc
	v_cndmask_b32_e32 v54, 0, v54, vcc
	v_cndmask_b32_e32 v55, 0, v55, vcc
	v_cmp_le_u32_e32 vcc, 13, v5
	s_nop 1
	v_cndmask_b32_e32 v56, 0, v56, vcc
	v_cndmask_b32_e32 v57, 0, v57, vcc
	v_cndmask_b32_e32 v58, 0, v58, vcc
	v_cndmask_b32_e32 v59, 0, v59, vcc
	v_cmp_le_u32_e32 vcc, 12, v5
	s_nop 1
	v_cndmask_b32_e32 v60, 0, v60, vcc
	v_cndmask_b32_e32 v61, 0, v61, vcc
	v_cndmask_b32_e32 v62, 0, v62, vcc
	v_cndmask_b32_e32 v63, 0, v63, vcc
	v_cmp_le_u32_e32 vcc, 11, v5
	s_nop 1
	v_cndmask_b32_e32 v64, 0, v64, vcc
	v_cndmask_b32_e32 v65, 0, v65, vcc
	v_cndmask_b32_e32 v66, 0, v66, vcc
	v_cndmask_b32_e32 v67, 0, v67, vcc
	v_cmp_le_u32_e32 vcc, 10, v5
	s_nop 1
	v_cndmask_b32_e32 v68, 0, v68, vcc
	v_cndmask_b32_e32 v69, 0, v69, vcc
	v_cndmask_b32_e32 v70, 0, v70, vcc
	v_cndmask_b32_e32 v71, 0, v71, vcc
	v_cmp_le_u32_e32 vcc, 9, v5
	s_nop 1
	v_cndmask_b32_e32 v72, 0, v72, vcc
	v_cndmask_b32_e32 v73, 0, v73, vcc
	v_cndmask_b32_e32 v74, 0, v74, vcc
	v_cndmask_b32_e32 v75, 0, v75, vcc
	v_cmp_le_u32_e32 vcc, 8, v5
	s_nop 1
	v_cndmask_b32_e32 v76, 0, v76, vcc
	v_cndmask_b32_e32 v77, 0, v77, vcc
	v_cndmask_b32_e32 v78, 0, v78, vcc
	v_cndmask_b32_e32 v79, 0, v79, vcc
	v_cmp_le_u32_e32 vcc, 7, v5
	s_nop 1
	v_cndmask_b32_e32 v80, 0, v80, vcc
	v_cndmask_b32_e32 v81, 0, v81, vcc
	v_cndmask_b32_e32 v82, 0, v82, vcc
	v_cndmask_b32_e32 v83, 0, v83, vcc
	v_cmp_le_u32_e32 vcc, 6, v5
	s_nop 1
	v_cndmask_b32_e32 v84, 0, v84, vcc
	v_cndmask_b32_e32 v85, 0, v85, vcc
	v_cndmask_b32_e32 v86, 0, v86, vcc
	v_cndmask_b32_e32 v87, 0, v87, vcc
	v_cmp_le_u32_e32 vcc, 5, v5
	s_nop 1
	v_cndmask_b32_e32 v88, 0, v88, vcc
	v_cndmask_b32_e32 v89, 0, v89, vcc
	v_cndmask_b32_e32 v90, 0, v90, vcc
	v_cndmask_b32_e32 v91, 0, v91, vcc
	v_cmp_le_u32_e32 vcc, 4, v5
	s_nop 1
	v_cndmask_b32_e32 v92, 0, v92, vcc
	v_cndmask_b32_e32 v93, 0, v93, vcc
	v_cndmask_b32_e32 v94, 0, v94, vcc
	v_cndmask_b32_e32 v95, 0, v95, vcc
	v_cmp_le_u32_e32 vcc, 3, v5
	s_nop 1
	v_cndmask_b32_e32 v96, 0, v96, vcc
	v_cndmask_b32_e32 v97, 0, v97, vcc
	v_cndmask_b32_e32 v98, 0, v98, vcc
	v_cndmask_b32_e32 v99, 0, v99, vcc
	v_cmp_le_u32_e32 vcc, 2, v5
	s_nop 1
	v_cndmask_b32_e32 v100, 0, v100, vcc
	v_cndmask_b32_e32 v101, 0, v101, vcc
	v_cndmask_b32_e32 v102, 0, v102, vcc
; __device__ __forceinline__ unsigned pk2(float lo, float hi) { return pg8::cvt_pk_bf16(lo, hi); }
; __device__ __forceinline__ void unpack8(const v4u w, float (&f)[8]) { f[0] = bflo(w.x); f[1] = bfhi(w.x); f[2] = bflo(w.y); f[3] = bfhi(w.y); f[4] = bflo(w.z); f[5] = bfhi(w.z); f[6] = bflo(w.w); f[7] = bfhi(w.w); }
; template <int W> __device__ __forceinline__ void pool_item(Frame& F, int row, int t, int c8) {
;     float s[8], u[8];
; #pragma unroll
;     for (int i = 0; i < 8; ++i) s[i] = 0.f;
;     v4u ld[W];
; #pragma unroll
;     for (int k = 0; k < W; ++k) { const int kk = (t - k) >= 0 ? k : t; ld[k] = *(const v4u*)(F.PROJ + (size_t)(row - kk) * INWP + O_UPOOL + c8); }
; #pragma unroll
;     for (int k = W - 1; k >= 0; --k) { unpack8(ld[k], u); const float wgt = (t - k) >= 0 ? 1.f : 0.f;
; #pragma unroll
;         for (int i = 0; i < 8; ++i) s[i] += wgt * u[i]; }
;     const int cnt = (t + 1) < W ? (t + 1) : W;
;     const float inv = 1.0f / (float)cnt;
;     v4u o; o.x = pk2(s[0] * inv - u[0], s[1] * inv - u[1]); o.y = pk2(s[2] * inv - u[2], s[3] * inv - u[3]); o.z = pk2(s[4] * inv - u[4], s[5] * inv - u[5]); o.w = pk2(s[6] * inv - u[6], s[7] * inv - u[7]);
;     *(v4u*)(F.Y + (size_t)row * 1024 + c8) = o;
; }
	v_cndmask_b32_e32 v103, 0, v103, vcc
	v_cmp_le_u32_e32 vcc, 1, v5
	s_nop 1
	v_cndmask_b32_e32 v104, 0, v104, vcc
	v_cndmask_b32_e32 v105, 0, v105, vcc
	v_cndmask_b32_e32 v106, 0, v106, vcc
	v_cndmask_b32_e32 v107, 0, v107, vcc
	v_add_u32_e32 v226, 1, v5
	v_min_u32_e32 v226, 16, v226
	v_cvt_f32_u32_e32 v226, v226
	v_rcp_f32_e32 v226, v226
	v_add_u32_e32 v227, 2, v5
	v_min_u32_e32 v227, 16, v227
	v_cvt_f32_u32_e32 v227, v227
	v_rcp_f32_e32 v227, v227
	v_add_u32_e32 v228, 3, v5
	v_min_u32_e32 v228, 16, v228
	v_cvt_f32_u32_e32 v228, v228
	v_rcp_f32_e32 v228, v228
	v_add_u32_e32 v229, 4, v5
	v_min_u32_e32 v229, 16, v229
	v_cvt_f32_u32_e32 v229, v229
	v_rcp_f32_e32 v229, v229
	v_lshlrev_b32_e32 v124, 16, v48
	v_and_b32_e32 v125, 0xffff0000, v48
	v_lshlrev_b32_e32 v126, 16, v52
	v_and_b32_e32 v127, 0xffff0000, v52
	v_lshlrev_b32_e32 v128, 16, v56
	v_and_b32_e32 v129, 0xffff0000, v56
	v_lshlrev_b32_e32 v130, 16, v60
	v_and_b32_e32 v131, 0xffff0000, v60
	v_lshlrev_b32_e32 v132, 16, v64
	v_and_b32_e32 v133, 0xffff0000, v64
	v_lshlrev_b32_e32 v134, 16, v68
	v_and_b32_e32 v135, 0xffff0000, v68
	v_lshlrev_b32_e32 v136, 16, v72
	v_and_b32_e32 v137, 0xffff0000, v72
	v_lshlrev_b32_e32 v138, 16, v76
	v_and_b32_e32 v139, 0xffff0000, v76
	v_lshlrev_b32_e32 v140, 16, v80
	v_and_b32_e32 v141, 0xffff0000, v80
	v_lshlrev_b32_e32 v142, 16, v84
	v_and_b32_e32 v143, 0xffff0000, v84
	v_lshlrev_b32_e32 v144, 16, v88
	v_and_b32_e32 v145, 0xffff0000, v88
	v_lshlrev_b32_e32 v146, 16, v92
	v_and_b32_e32 v147, 0xffff0000, v92
	v_lshlrev_b32_e32 v148, 16, v96
	v_and_b32_e32 v149, 0xffff0000, v96
	v_lshlrev_b32_e32 v150, 16, v100
	v_and_b32_e32 v151, 0xffff0000, v100
	v_lshlrev_b32_e32 v152, 16, v104
	v_and_b32_e32 v153, 0xffff0000, v104
	v_lshlrev_b32_e32 v154, 16, v108
	v_and_b32_e32 v155, 0xffff0000, v108
	v_lshlrev_b32_e32 v156, 16, v112
	v_and_b32_e32 v157, 0xffff0000, v112
	v_lshlrev_b32_e32 v158, 16, v116
	v_and_b32_e32 v159, 0xffff0000, v116
	v_lshlrev_b32_e32 v160, 16, v120
	v_and_b32_e32 v161, 0xffff0000, v120
	v_add_f32_e32 v194, v124, v126
	v_add_f32_e32 v194, v194, v128
	v_add_f32_e32 v194, v194, v130
	v_add_f32_e32 v194, v194, v132
	v_add_f32_e32 v194, v194, v134
	v_add_f32_e32 v194, v194, v136
	v_add_f32_e32 v194, v194, v138
	v_add_f32_e32 v194, v194, v140
	v_add_f32_e32 v194, v194, v142
	v_add_f32_e32 v194, v194, v144
	v_add_f32_e32 v194, v194, v146
	v_add_f32_e32 v194, v194, v148
	v_add_f32_e32 v194, v194, v150
	v_add_f32_e32 v194, v194, v152
	v_add_f32_e32 v194, v194, v154
	v_fma_f32 v194, v194, v226, -v154
	v_add_f32_e32 v195, v125, v127
	v_add_f32_e32 v195, v195, v129
	v_add_f32_e32 v195, v195, v131
	v_add_f32_e32 v195, v195, v133
	v_add_f32_e32 v195, v195, v135
	v_add_f32_e32 v195, v195, v137
	v_add_f32_e32 v195, v195, v139
	v_add_f32_e32 v195, v195, v141
	v_add_f32_e32 v195, v195, v143
	v_add_f32_e32 v195, v195, v145
	v_add_f32_e32 v195, v195, v147
	v_add_f32_e32 v195, v195, v149
	v_add_f32_e32 v195, v195, v151
	v_add_f32_e32 v195, v195, v153
	v_add_f32_e32 v195, v195, v155
	v_fma_f32 v195, v195, v226, -v155
	v_add_f32_e32 v202, v126, v128
	v_add_f32_e32 v202, v202, v130
	v_add_f32_e32 v202, v202, v132
	v_add_f32_e32 v202, v202, v134
	v_add_f32_e32 v202, v202, v136
	v_add_f32_e32 v202, v202, v138
	v_add_f32_e32 v202, v202, v140
	v_add_f32_e32 v202, v202, v142
	v_add_f32_e32 v202, v202, v144
	v_add_f32_e32 v202, v202, v146
	v_add_f32_e32 v202, v202, v148
	v_add_f32_e32 v202, v202, v150
	v_add_f32_e32 v202, v202, v152
	v_add_f32_e32 v202, v202, v154
	v_add_f32_e32 v202, v202, v156
	v_fma_f32 v202, v202, v227, -v156
	v_add_f32_e32 v203, v127, v129
	v_add_f32_e32 v203, v203, v131
	v_add_f32_e32 v203, v203, v133
	v_add_f32_e32 v203, v203, v135
	v_add_f32_e32 v203, v203, v137
	v_add_f32_e32 v203, v203, v139
	v_add_f32_e32 v203, v203, v141
	v_add_f32_e32 v203, v203, v143
	v_add_f32_e32 v203, v203, v145
	v_add_f32_e32 v203, v203, v147
	v_add_f32_e32 v203, v203, v149
	v_add_f32_e32 v203, v203, v151
	v_add_f32_e32 v203, v203, v153
	v_add_f32_e32 v203, v203, v155
	v_add_f32_e32 v203, v203, v157
	v_fma_f32 v203, v203, v227, -v157
	v_add_f32_e32 v210, v128, v130
	v_add_f32_e32 v210, v210, v132
	v_add_f32_e32 v210, v210, v134
	v_add_f32_e32 v210, v210, v136
	v_add_f32_e32 v210, v210, v138
	v_add_f32_e32 v210, v210, v140
	v_add_f32_e32 v210, v210, v142
	v_add_f32_e32 v210, v210, v144
	v_add_f32_e32 v210, v210, v146
	v_add_f32_e32 v210, v210, v148
	v_add_f32_e32 v210, v210, v150
	v_add_f32_e32 v210, v210, v152
	v_add_f32_e32 v210, v210, v154
	v_add_f32_e32 v210, v210, v156
	v_add_f32_e32 v210, v210, v158
	v_fma_f32 v210, v210, v228, -v158
	v_add_f32_e32 v211, v129, v131
	v_add_f32_e32 v211, v211, v133
	v_add_f32_e32 v211, v211, v135
	v_add_f32_e32 v211, v211, v137
	v_add_f32_e32 v211, v211, v139
	v_add_f32_e32 v211, v211, v141
	v_add_f32_e32 v211, v211, v143
	v_add_f32_e32 v211, v211, v145
	v_add_f32_e32 v211, v211, v147
	v_add_f32_e32 v211, v211, v149
	v_add_f32_e32 v211, v211, v151
	v_add_f32_e32 v211, v211, v153
	v_add_f32_e32 v211, v211, v155
	v_add_f32_e32 v211, v211, v157
	v_add_f32_e32 v211, v211, v159
	v_fma_f32 v211, v211, v228, -v159
	v_add_f32_e32 v218, v130, v132
	v_add_f32_e32 v218, v218, v134
	v_add_f32_e32 v218, v218, v136
	v_add_f32_e32 v218, v218, v138
	v_add_f32_e32 v218, v218, v140
	v_add_f32_e32 v218, v218, v142
	v_add_f32_e32 v218, v218, v144
	v_add_f32_e32 v218, v218, v146
	v_add_f32_e32 v218, v218, v148
	v_add_f32_e32 v218, v218, v150
	v_add_f32_e32 v218, v218, v152
	v_add_f32_e32 v218, v218, v154
	v_add_f32_e32 v218, v218, v156
	v_add_f32_e32 v218, v218, v158
	v_add_f32_e32 v218, v218, v160
	v_fma_f32 v218, v218, v229, -v160
; __device__ __forceinline__ unsigned pk2(float lo, float hi) { return pg8::cvt_pk_bf16(lo, hi); }
; __device__ __forceinline__ void unpack8(const v4u w, float (&f)[8]) { f[0] = bflo(w.x); f[1] = bfhi(w.x); f[2] = bflo(w.y); f[3] = bfhi(w.y); f[4] = bflo(w.z); f[5] = bfhi(w.z); f[6] = bflo(w.w); f[7] = bfhi(w.w); }
; template <int W> __device__ __forceinline__ void pool_item(Frame& F, int row, int t, int c8) {
;     float s[8], u[8];
; #pragma unroll
;     for (int i = 0; i < 8; ++i) s[i] = 0.f;
;     v4u ld[W];
; #pragma unroll
;     for (int k = 0; k < W; ++k) { const int kk = (t - k) >= 0 ? k : t; ld[k] = *(const v4u*)(F.PROJ + (size_t)(row - kk) * INWP + O_UPOOL + c8); }
; #pragma unroll
;     for (int k = W - 1; k >= 0; --k) { unpack8(ld[k], u); const float wgt = (t - k) >= 0 ? 1.f : 0.f;
; #pragma unroll
;         for (int i = 0; i < 8; ++i) s[i] += wgt * u[i]; }
;     const int cnt = (t + 1) < W ? (t + 1) : W;
;     const float inv = 1.0f / (float)cnt;
;     v4u o; o.x = pk2(s[0] * inv - u[0], s[1] * inv - u[1]); o.y = pk2(s[2] * inv - u[2], s[3] * inv - u[3]); o.z = pk2(s[4] * inv - u[4], s[5] * inv - u[5]); o.w = pk2(s[6] * inv - u[6], s[7] * inv - u[7]);
;     *(v4u*)(F.Y + (size_t)row * 1024 + c8) = o;
; }
	v_add_f32_e32 v219, v131, v133
	v_add_f32_e32 v219, v219, v135
	v_add_f32_e32 v219, v219, v137
	v_add_f32_e32 v219, v219, v139
	v_add_f32_e32 v219, v219, v141
	v_add_f32_e32 v219, v219, v143
	v_add_f32_e32 v219, v219, v145
	v_add_f32_e32 v219, v219, v147
	v_add_f32_e32 v219, v219, v149
	v_add_f32_e32 v219, v219, v151
	v_add_f32_e32 v219, v219, v153
	v_add_f32_e32 v219, v219, v155
	v_add_f32_e32 v219, v219, v157
	v_add_f32_e32 v219, v219, v159
	v_add_f32_e32 v219, v219, v161
	v_fma_f32 v219, v219, v229, -v161
	v_lshlrev_b32_e32 v124, 16, v49
	v_and_b32_e32 v125, 0xffff0000, v49
	v_lshlrev_b32_e32 v126, 16, v53
	v_and_b32_e32 v127, 0xffff0000, v53
	v_lshlrev_b32_e32 v128, 16, v57
	v_and_b32_e32 v129, 0xffff0000, v57
	v_lshlrev_b32_e32 v130, 16, v61
	v_and_b32_e32 v131, 0xffff0000, v61
	v_lshlrev_b32_e32 v132, 16, v65
	v_and_b32_e32 v133, 0xffff0000, v65
	v_lshlrev_b32_e32 v134, 16, v69
	v_and_b32_e32 v135, 0xffff0000, v69
	v_lshlrev_b32_e32 v136, 16, v73
	v_and_b32_e32 v137, 0xffff0000, v73
	v_lshlrev_b32_e32 v138, 16, v77
	v_and_b32_e32 v139, 0xffff0000, v77
	v_lshlrev_b32_e32 v140, 16, v81
	v_and_b32_e32 v141, 0xffff0000, v81
	v_lshlrev_b32_e32 v142, 16, v85
	v_and_b32_e32 v143, 0xffff0000, v85
	v_lshlrev_b32_e32 v144, 16, v89
	v_and_b32_e32 v145, 0xffff0000, v89
	v_lshlrev_b32_e32 v146, 16, v93
	v_and_b32_e32 v147, 0xffff0000, v93
	v_lshlrev_b32_e32 v148, 16, v97
	v_and_b32_e32 v149, 0xffff0000, v97
	v_lshlrev_b32_e32 v150, 16, v101
	v_and_b32_e32 v151, 0xffff0000, v101
	v_lshlrev_b32_e32 v152, 16, v105
	v_and_b32_e32 v153, 0xffff0000, v105
	v_lshlrev_b32_e32 v154, 16, v109
	v_and_b32_e32 v155, 0xffff0000, v109
	v_lshlrev_b32_e32 v156, 16, v113
	v_and_b32_e32 v157, 0xffff0000, v113
	v_lshlrev_b32_e32 v158, 16, v117
	v_and_b32_e32 v159, 0xffff0000, v117
	v_lshlrev_b32_e32 v160, 16, v121
	v_and_b32_e32 v161, 0xffff0000, v121
	v_add_f32_e32 v196, v124, v126
	v_add_f32_e32 v196, v196, v128
	v_add_f32_e32 v196, v196, v130
	v_add_f32_e32 v196, v196, v132
	v_add_f32_e32 v196, v196, v134
	v_add_f32_e32 v196, v196, v136
	v_add_f32_e32 v196, v196, v138
	v_add_f32_e32 v196, v196, v140
	v_add_f32_e32 v196, v196, v142
	v_add_f32_e32 v196, v196, v144
	v_add_f32_e32 v196, v196, v146
	v_add_f32_e32 v196, v196, v148
	v_add_f32_e32 v196, v196, v150
	v_add_f32_e32 v196, v196, v152
	v_add_f32_e32 v196, v196, v154
	v_fma_f32 v196, v196, v226, -v154
	v_add_f32_e32 v197, v125, v127
	v_add_f32_e32 v197, v197, v129
	v_add_f32_e32 v197, v197, v131
	v_add_f32_e32 v197, v197, v133
	v_add_f32_e32 v197, v197, v135
	v_add_f32_e32 v197, v197, v137
	v_add_f32_e32 v197, v197, v139
	v_add_f32_e32 v197, v197, v141
	v_add_f32_e32 v197, v197, v143
	v_add_f32_e32 v197, v197, v145
	v_add_f32_e32 v197, v197, v147
	v_add_f32_e32 v197, v197, v149
	v_add_f32_e32 v197, v197, v151
	v_add_f32_e32 v197, v197, v153
	v_add_f32_e32 v197, v197, v155
	v_fma_f32 v197, v197, v226, -v155
	v_add_f32_e32 v204, v126, v128
	v_add_f32_e32 v204, v204, v130
	v_add_f32_e32 v204, v204, v132
	v_add_f32_e32 v204, v204, v134
	v_add_f32_e32 v204, v204, v136
	v_add_f32_e32 v204, v204, v138
	v_add_f32_e32 v204, v204, v140
	v_add_f32_e32 v204, v204, v142
	v_add_f32_e32 v204, v204, v144
	v_add_f32_e32 v204, v204, v146
	v_add_f32_e32 v204, v204, v148
	v_add_f32_e32 v204, v204, v150
	v_add_f32_e32 v204, v204, v152
	v_add_f32_e32 v204, v204, v154
	v_add_f32_e32 v204, v204, v156
	v_fma_f32 v204, v204, v227, -v156
	v_add_f32_e32 v205, v127, v129
	v_add_f32_e32 v205, v205, v131
	v_add_f32_e32 v205, v205, v133
	v_add_f32_e32 v205, v205, v135
	v_add_f32_e32 v205, v205, v137
	v_add_f32_e32 v205, v205, v139
	v_add_f32_e32 v205, v205, v141
	v_add_f32_e32 v205, v205, v143
	v_add_f32_e32 v205, v205, v145
	v_add_f32_e32 v205, v205, v147
	v_add_f32_e32 v205, v205, v149
	v_add_f32_e32 v205, v205, v151
	v_add_f32_e32 v205, v205, v153
	v_add_f32_e32 v205, v205, v155
	v_add_f32_e32 v205, v205, v157
	v_fma_f32 v205, v205, v227, -v157
	v_add_f32_e32 v212, v128, v130
	v_add_f32_e32 v212, v212, v132
	v_add_f32_e32 v212, v212, v134
	v_add_f32_e32 v212, v212, v136
	v_add_f32_e32 v212, v212, v138
	v_add_f32_e32 v212, v212, v140
	v_add_f32_e32 v212, v212, v142
	v_add_f32_e32 v212, v212, v144
	v_add_f32_e32 v212, v212, v146
	v_add_f32_e32 v212, v212, v148
	v_add_f32_e32 v212, v212, v150
	v_add_f32_e32 v212, v212, v152
	v_add_f32_e32 v212, v212, v154
	v_add_f32_e32 v212, v212, v156
	v_add_f32_e32 v212, v212, v158
	v_fma_f32 v212, v212, v228, -v158
	v_add_f32_e32 v213, v129, v131
	v_add_f32_e32 v213, v213, v133
	v_add_f32_e32 v213, v213, v135
	v_add_f32_e32 v213, v213, v137
	v_add_f32_e32 v213, v213, v139
	v_add_f32_e32 v213, v213, v141
	v_add_f32_e32 v213, v213, v143
	v_add_f32_e32 v213, v213, v145
	v_add_f32_e32 v213, v213, v147
	v_add_f32_e32 v213, v213, v149
	v_add_f32_e32 v213, v213, v151
	v_add_f32_e32 v213, v213, v153
	v_add_f32_e32 v213, v213, v155
	v_add_f32_e32 v213, v213, v157
	v_add_f32_e32 v213, v213, v159
	v_fma_f32 v213, v213, v228, -v159
	v_add_f32_e32 v220, v130, v132
	v_add_f32_e32 v220, v220, v134
	v_add_f32_e32 v220, v220, v136
	v_add_f32_e32 v220, v220, v138
	v_add_f32_e32 v220, v220, v140
	v_add_f32_e32 v220, v220, v142
	v_add_f32_e32 v220, v220, v144
	v_add_f32_e32 v220, v220, v146
	v_add_f32_e32 v220, v220, v148
	v_add_f32_e32 v220, v220, v150
	v_add_f32_e32 v220, v220, v152
	v_add_f32_e32 v220, v220, v154
	v_add_f32_e32 v220, v220, v156
	v_add_f32_e32 v220, v220, v158
	v_add_f32_e32 v220, v220, v160
	v_fma_f32 v220, v220, v229, -v160
	v_add_f32_e32 v221, v131, v133
	v_add_f32_e32 v221, v221, v135
	v_add_f32_e32 v221, v221, v137
	v_add_f32_e32 v221, v221, v139
	v_add_f32_e32 v221, v221, v141
	v_add_f32_e32 v221, v221, v143
; __device__ __forceinline__ unsigned pk2(float lo, float hi) { return pg8::cvt_pk_bf16(lo, hi); }
; __device__ __forceinline__ void unpack8(const v4u w, float (&f)[8]) { f[0] = bflo(w.x); f[1] = bfhi(w.x); f[2] = bflo(w.y); f[3] = bfhi(w.y); f[4] = bflo(w.z); f[5] = bfhi(w.z); f[6] = bflo(w.w); f[7] = bfhi(w.w); }
; template <int W> __device__ __forceinline__ void pool_item(Frame& F, int row, int t, int c8) {
;     float s[8], u[8];
; #pragma unroll
;     for (int i = 0; i < 8; ++i) s[i] = 0.f;
;     v4u ld[W];
; #pragma unroll
;     for (int k = 0; k < W; ++k) { const int kk = (t - k) >= 0 ? k : t; ld[k] = *(const v4u*)(F.PROJ + (size_t)(row - kk) * INWP + O_UPOOL + c8); }
; #pragma unroll
;     for (int k = W - 1; k >= 0; --k) { unpack8(ld[k], u); const float wgt = (t - k) >= 0 ? 1.f : 0.f;
; #pragma unroll
;         for (int i = 0; i < 8; ++i) s[i] += wgt * u[i]; }
;     const int cnt = (t + 1) < W ? (t + 1) : W;
;     const float inv = 1.0f / (float)cnt;
;     v4u o; o.x = pk2(s[0] * inv - u[0], s[1] * inv - u[1]); o.y = pk2(s[2] * inv - u[2], s[3] * inv - u[3]); o.z = pk2(s[4] * inv - u[4], s[5] * inv - u[5]); o.w = pk2(s[6] * inv - u[6], s[7] * inv - u[7]);
;     *(v4u*)(F.Y + (size_t)row * 1024 + c8) = o;
; }
	v_add_f32_e32 v221, v221, v145
	v_add_f32_e32 v221, v221, v147
	v_add_f32_e32 v221, v221, v149
	v_add_f32_e32 v221, v221, v151
	v_add_f32_e32 v221, v221, v153
	v_add_f32_e32 v221, v221, v155
	v_add_f32_e32 v221, v221, v157
	v_add_f32_e32 v221, v221, v159
	v_add_f32_e32 v221, v221, v161
	v_fma_f32 v221, v221, v229, -v161
	v_lshlrev_b32_e32 v124, 16, v50
	v_and_b32_e32 v125, 0xffff0000, v50
	v_lshlrev_b32_e32 v126, 16, v54
	v_and_b32_e32 v127, 0xffff0000, v54
	v_lshlrev_b32_e32 v128, 16, v58
	v_and_b32_e32 v129, 0xffff0000, v58
	v_lshlrev_b32_e32 v130, 16, v62
	v_and_b32_e32 v131, 0xffff0000, v62
	v_lshlrev_b32_e32 v132, 16, v66
	v_and_b32_e32 v133, 0xffff0000, v66
	v_lshlrev_b32_e32 v134, 16, v70
	v_and_b32_e32 v135, 0xffff0000, v70
	v_lshlrev_b32_e32 v136, 16, v74
	v_and_b32_e32 v137, 0xffff0000, v74
	v_lshlrev_b32_e32 v138, 16, v78
	v_and_b32_e32 v139, 0xffff0000, v78
	v_lshlrev_b32_e32 v140, 16, v82
	v_and_b32_e32 v141, 0xffff0000, v82
	v_lshlrev_b32_e32 v142, 16, v86
	v_and_b32_e32 v143, 0xffff0000, v86
	v_lshlrev_b32_e32 v144, 16, v90
	v_and_b32_e32 v145, 0xffff0000, v90
	v_lshlrev_b32_e32 v146, 16, v94
	v_and_b32_e32 v147, 0xffff0000, v94
	v_lshlrev_b32_e32 v148, 16, v98
	v_and_b32_e32 v149, 0xffff0000, v98
	v_lshlrev_b32_e32 v150, 16, v102
	v_and_b32_e32 v151, 0xffff0000, v102
	v_lshlrev_b32_e32 v152, 16, v106
	v_and_b32_e32 v153, 0xffff0000, v106
	v_lshlrev_b32_e32 v154, 16, v110
	v_and_b32_e32 v155, 0xffff0000, v110
	v_lshlrev_b32_e32 v156, 16, v114
	v_and_b32_e32 v157, 0xffff0000, v114
	v_lshlrev_b32_e32 v158, 16, v118
	v_and_b32_e32 v159, 0xffff0000, v118
	v_lshlrev_b32_e32 v160, 16, v122
	v_and_b32_e32 v161, 0xffff0000, v122
	v_add_f32_e32 v198, v124, v126
	v_add_f32_e32 v198, v198, v128
	v_add_f32_e32 v198, v198, v130
	v_add_f32_e32 v198, v198, v132
	v_add_f32_e32 v198, v198, v134
	v_add_f32_e32 v198, v198, v136
	v_add_f32_e32 v198, v198, v138
	v_add_f32_e32 v198, v198, v140
	v_add_f32_e32 v198, v198, v142
	v_add_f32_e32 v198, v198, v144
	v_add_f32_e32 v198, v198, v146
	v_add_f32_e32 v198, v198, v148
	v_add_f32_e32 v198, v198, v150
	v_add_f32_e32 v198, v198, v152
	v_add_f32_e32 v198, v198, v154
	v_fma_f32 v198, v198, v226, -v154
	v_add_f32_e32 v199, v125, v127
	v_add_f32_e32 v199, v199, v129
	v_add_f32_e32 v199, v199, v131
	v_add_f32_e32 v199, v199, v133
	v_add_f32_e32 v199, v199, v135
	v_add_f32_e32 v199, v199, v137
	v_add_f32_e32 v199, v199, v139
	v_add_f32_e32 v199, v199, v141
	v_add_f32_e32 v199, v199, v143
	v_add_f32_e32 v199, v199, v145
	v_add_f32_e32 v199, v199, v147
	v_add_f32_e32 v199, v199, v149
	v_add_f32_e32 v199, v199, v151
	v_add_f32_e32 v199, v199, v153
	v_add_f32_e32 v199, v199, v155
	v_fma_f32 v199, v199, v226, -v155
	v_add_f32_e32 v206, v126, v128
	v_add_f32_e32 v206, v206, v130
	v_add_f32_e32 v206, v206, v132
	v_add_f32_e32 v206, v206, v134
	v_add_f32_e32 v206, v206, v136
	v_add_f32_e32 v206, v206, v138
	v_add_f32_e32 v206, v206, v140
	v_add_f32_e32 v206, v206, v142
	v_add_f32_e32 v206, v206, v144
	v_add_f32_e32 v206, v206, v146
	v_add_f32_e32 v206, v206, v148
	v_add_f32_e32 v206, v206, v150
	v_add_f32_e32 v206, v206, v152
	v_add_f32_e32 v206, v206, v154
	v_add_f32_e32 v206, v206, v156
	v_fma_f32 v206, v206, v227, -v156
	v_add_f32_e32 v207, v127, v129
	v_add_f32_e32 v207, v207, v131
	v_add_f32_e32 v207, v207, v133
	v_add_f32_e32 v207, v207, v135
	v_add_f32_e32 v207, v207, v137
	v_add_f32_e32 v207, v207, v139
	v_add_f32_e32 v207, v207, v141
	v_add_f32_e32 v207, v207, v143
	v_add_f32_e32 v207, v207, v145
	v_add_f32_e32 v207, v207, v147
	v_add_f32_e32 v207, v207, v149
	v_add_f32_e32 v207, v207, v151
	v_add_f32_e32 v207, v207, v153
	v_add_f32_e32 v207, v207, v155
	v_add_f32_e32 v207, v207, v157
	v_fma_f32 v207, v207, v227, -v157
	v_add_f32_e32 v214, v128, v130
	v_add_f32_e32 v214, v214, v132
	v_add_f32_e32 v214, v214, v134
	v_add_f32_e32 v214, v214, v136
	v_add_f32_e32 v214, v214, v138
	v_add_f32_e32 v214, v214, v140
	v_add_f32_e32 v214, v214, v142
	v_add_f32_e32 v214, v214, v144
	v_add_f32_e32 v214, v214, v146
	v_add_f32_e32 v214, v214, v148
	v_add_f32_e32 v214, v214, v150
	v_add_f32_e32 v214, v214, v152
	v_add_f32_e32 v214, v214, v154
	v_add_f32_e32 v214, v214, v156
	v_add_f32_e32 v214, v214, v158
	v_fma_f32 v214, v214, v228, -v158
	v_add_f32_e32 v215, v129, v131
	v_add_f32_e32 v215, v215, v133
	v_add_f32_e32 v215, v215, v135
	v_add_f32_e32 v215, v215, v137
	v_add_f32_e32 v215, v215, v139
	v_add_f32_e32 v215, v215, v141
	v_add_f32_e32 v215, v215, v143
	v_add_f32_e32 v215, v215, v145
	v_add_f32_e32 v215, v215, v147
	v_add_f32_e32 v215, v215, v149
	v_add_f32_e32 v215, v215, v151
	v_add_f32_e32 v215, v215, v153
	v_add_f32_e32 v215, v215, v155
	v_add_f32_e32 v215, v215, v157
	v_add_f32_e32 v215, v215, v159
	v_fma_f32 v215, v215, v228, -v159
	v_add_f32_e32 v222, v130, v132
	v_add_f32_e32 v222, v222, v134
	v_add_f32_e32 v222, v222, v136
	v_add_f32_e32 v222, v222, v138
	v_add_f32_e32 v222, v222, v140
	v_add_f32_e32 v222, v222, v142
	v_add_f32_e32 v222, v222, v144
	v_add_f32_e32 v222, v222, v146
	v_add_f32_e32 v222, v222, v148
	v_add_f32_e32 v222, v222, v150
	v_add_f32_e32 v222, v222, v152
	v_add_f32_e32 v222, v222, v154
	v_add_f32_e32 v222, v222, v156
	v_add_f32_e32 v222, v222, v158
	v_add_f32_e32 v222, v222, v160
	v_fma_f32 v222, v222, v229, -v160
	v_add_f32_e32 v223, v131, v133
	v_add_f32_e32 v223, v223, v135
	v_add_f32_e32 v223, v223, v137
	v_add_f32_e32 v223, v223, v139
	v_add_f32_e32 v223, v223, v141
	v_add_f32_e32 v223, v223, v143
	v_add_f32_e32 v223, v223, v145
	v_add_f32_e32 v223, v223, v147
	v_add_f32_e32 v223, v223, v149
	v_add_f32_e32 v223, v223, v151
	v_add_f32_e32 v223, v223, v153
	v_add_f32_e32 v223, v223, v155
; __device__ __forceinline__ unsigned pk2(float lo, float hi) { return pg8::cvt_pk_bf16(lo, hi); }
; __device__ __forceinline__ void unpack8(const v4u w, float (&f)[8]) { f[0] = bflo(w.x); f[1] = bfhi(w.x); f[2] = bflo(w.y); f[3] = bfhi(w.y); f[4] = bflo(w.z); f[5] = bfhi(w.z); f[6] = bflo(w.w); f[7] = bfhi(w.w); }
; template <int W> __device__ __forceinline__ void pool_item(Frame& F, int row, int t, int c8) {
;     float s[8], u[8];
; #pragma unroll
;     for (int i = 0; i < 8; ++i) s[i] = 0.f;
;     v4u ld[W];
; #pragma unroll
;     for (int k = 0; k < W; ++k) { const int kk = (t - k) >= 0 ? k : t; ld[k] = *(const v4u*)(F.PROJ + (size_t)(row - kk) * INWP + O_UPOOL + c8); }
; #pragma unroll
;     for (int k = W - 1; k >= 0; --k) { unpack8(ld[k], u); const float wgt = (t - k) >= 0 ? 1.f : 0.f;
; #pragma unroll
;         for (int i = 0; i < 8; ++i) s[i] += wgt * u[i]; }
;     const int cnt = (t + 1) < W ? (t + 1) : W;
;     const float inv = 1.0f / (float)cnt;
;     v4u o; o.x = pk2(s[0] * inv - u[0], s[1] * inv - u[1]); o.y = pk2(s[2] * inv - u[2], s[3] * inv - u[3]); o.z = pk2(s[4] * inv - u[4], s[5] * inv - u[5]); o.w = pk2(s[6] * inv - u[6], s[7] * inv - u[7]);
;     *(v4u*)(F.Y + (size_t)row * 1024 + c8) = o;
; }
	v_add_f32_e32 v223, v223, v157
	v_add_f32_e32 v223, v223, v159
	v_add_f32_e32 v223, v223, v161
	v_fma_f32 v223, v223, v229, -v161
	v_lshlrev_b32_e32 v124, 16, v51
	v_and_b32_e32 v125, 0xffff0000, v51
	v_lshlrev_b32_e32 v126, 16, v55
	v_and_b32_e32 v127, 0xffff0000, v55
	v_lshlrev_b32_e32 v128, 16, v59
	v_and_b32_e32 v129, 0xffff0000, v59
	v_lshlrev_b32_e32 v130, 16, v63
	v_and_b32_e32 v131, 0xffff0000, v63
	v_lshlrev_b32_e32 v132, 16, v67
	v_and_b32_e32 v133, 0xffff0000, v67
	v_lshlrev_b32_e32 v134, 16, v71
	v_and_b32_e32 v135, 0xffff0000, v71
	v_lshlrev_b32_e32 v136, 16, v75
	v_and_b32_e32 v137, 0xffff0000, v75
	v_lshlrev_b32_e32 v138, 16, v79
	v_and_b32_e32 v139, 0xffff0000, v79
	v_lshlrev_b32_e32 v140, 16, v83
	v_and_b32_e32 v141, 0xffff0000, v83
	v_lshlrev_b32_e32 v142, 16, v87
	v_and_b32_e32 v143, 0xffff0000, v87
	v_lshlrev_b32_e32 v144, 16, v91
	v_and_b32_e32 v145, 0xffff0000, v91
	v_lshlrev_b32_e32 v146, 16, v95
	v_and_b32_e32 v147, 0xffff0000, v95
	v_lshlrev_b32_e32 v148, 16, v99
	v_and_b32_e32 v149, 0xffff0000, v99
	v_lshlrev_b32_e32 v150, 16, v103
	v_and_b32_e32 v151, 0xffff0000, v103
	v_lshlrev_b32_e32 v152, 16, v107
	v_and_b32_e32 v153, 0xffff0000, v107
	v_lshlrev_b32_e32 v154, 16, v111
	v_and_b32_e32 v155, 0xffff0000, v111
	v_lshlrev_b32_e32 v156, 16, v115
	v_and_b32_e32 v157, 0xffff0000, v115
	v_lshlrev_b32_e32 v158, 16, v119
	v_and_b32_e32 v159, 0xffff0000, v119
	v_lshlrev_b32_e32 v160, 16, v123
	v_and_b32_e32 v161, 0xffff0000, v123
	v_add_f32_e32 v200, v124, v126
	v_add_f32_e32 v200, v200, v128
	v_add_f32_e32 v200, v200, v130
	v_add_f32_e32 v200, v200, v132
	v_add_f32_e32 v200, v200, v134
	v_add_f32_e32 v200, v200, v136
	v_add_f32_e32 v200, v200, v138
	v_add_f32_e32 v200, v200, v140
	v_add_f32_e32 v200, v200, v142
	v_add_f32_e32 v200, v200, v144
	v_add_f32_e32 v200, v200, v146
	v_add_f32_e32 v200, v200, v148
	v_add_f32_e32 v200, v200, v150
	v_add_f32_e32 v200, v200, v152
	v_add_f32_e32 v200, v200, v154
	v_fma_f32 v200, v200, v226, -v154
	v_add_f32_e32 v201, v125, v127
	v_add_f32_e32 v201, v201, v129
	v_add_f32_e32 v201, v201, v131
	v_add_f32_e32 v201, v201, v133
	v_add_f32_e32 v201, v201, v135
	v_add_f32_e32 v201, v201, v137
	v_add_f32_e32 v201, v201, v139
	v_add_f32_e32 v201, v201, v141
	v_add_f32_e32 v201, v201, v143
	v_add_f32_e32 v201, v201, v145
	v_add_f32_e32 v201, v201, v147
	v_add_f32_e32 v201, v201, v149
	v_add_f32_e32 v201, v201, v151
	v_add_f32_e32 v201, v201, v153
	v_add_f32_e32 v201, v201, v155
	v_fma_f32 v201, v201, v226, -v155
	v_add_f32_e32 v208, v126, v128
	v_add_f32_e32 v208, v208, v130
	v_add_f32_e32 v208, v208, v132
	v_add_f32_e32 v208, v208, v134
	v_add_f32_e32 v208, v208, v136
	v_add_f32_e32 v208, v208, v138
	v_add_f32_e32 v208, v208, v140
	v_add_f32_e32 v208, v208, v142
	v_add_f32_e32 v208, v208, v144
	v_add_f32_e32 v208, v208, v146
	v_add_f32_e32 v208, v208, v148
	v_add_f32_e32 v208, v208, v150
	v_add_f32_e32 v208, v208, v152
	v_add_f32_e32 v208, v208, v154
	v_add_f32_e32 v208, v208, v156
	v_fma_f32 v208, v208, v227, -v156
	v_add_f32_e32 v209, v127, v129
	v_add_f32_e32 v209, v209, v131
	v_add_f32_e32 v209, v209, v133
	v_add_f32_e32 v209, v209, v135
	v_add_f32_e32 v209, v209, v137
	v_add_f32_e32 v209, v209, v139
	v_add_f32_e32 v209, v209, v141
	v_add_f32_e32 v209, v209, v143
	v_add_f32_e32 v209, v209, v145
	v_add_f32_e32 v209, v209, v147
	v_add_f32_e32 v209, v209, v149
	v_add_f32_e32 v209, v209, v151
	v_add_f32_e32 v209, v209, v153
	v_add_f32_e32 v209, v209, v155
	v_add_f32_e32 v209, v209, v157
	v_fma_f32 v209, v209, v227, -v157
	v_add_f32_e32 v216, v128, v130
	v_add_f32_e32 v216, v216, v132
	v_add_f32_e32 v216, v216, v134
	v_add_f32_e32 v216, v216, v136
	v_add_f32_e32 v216, v216, v138
	v_add_f32_e32 v216, v216, v140
	v_add_f32_e32 v216, v216, v142
	v_add_f32_e32 v216, v216, v144
	v_add_f32_e32 v216, v216, v146
	v_add_f32_e32 v216, v216, v148
	v_add_f32_e32 v216, v216, v150
	v_add_f32_e32 v216, v216, v152
	v_add_f32_e32 v216, v216, v154
	v_add_f32_e32 v216, v216, v156
	v_add_f32_e32 v216, v216, v158
	v_fma_f32 v216, v216, v228, -v158
	v_add_f32_e32 v217, v129, v131
	v_add_f32_e32 v217, v217, v133
	v_add_f32_e32 v217, v217, v135
	v_add_f32_e32 v217, v217, v137
	v_add_f32_e32 v217, v217, v139
	v_add_f32_e32 v217, v217, v141
	v_add_f32_e32 v217, v217, v143
	v_add_f32_e32 v217, v217, v145
	v_add_f32_e32 v217, v217, v147
	v_add_f32_e32 v217, v217, v149
	v_add_f32_e32 v217, v217, v151
	v_add_f32_e32 v217, v217, v153
	v_add_f32_e32 v217, v217, v155
	v_add_f32_e32 v217, v217, v157
	v_add_f32_e32 v217, v217, v159
	v_fma_f32 v217, v217, v228, -v159
	v_add_f32_e32 v224, v130, v132
	v_add_f32_e32 v224, v224, v134
	v_add_f32_e32 v224, v224, v136
	v_add_f32_e32 v224, v224, v138
	v_add_f32_e32 v224, v224, v140
	v_add_f32_e32 v224, v224, v142
	v_add_f32_e32 v224, v224, v144
	v_add_f32_e32 v224, v224, v146
	v_add_f32_e32 v224, v224, v148
	v_add_f32_e32 v224, v224, v150
	v_add_f32_e32 v224, v224, v152
	v_add_f32_e32 v224, v224, v154
	v_add_f32_e32 v224, v224, v156
	v_add_f32_e32 v224, v224, v158
	v_add_f32_e32 v224, v224, v160
	v_fma_f32 v224, v224, v229, -v160
	v_add_f32_e32 v225, v131, v133
	v_add_f32_e32 v225, v225, v135
	v_add_f32_e32 v225, v225, v137
	v_add_f32_e32 v225, v225, v139
	v_add_f32_e32 v225, v225, v141
	v_add_f32_e32 v225, v225, v143
	v_add_f32_e32 v225, v225, v145
	v_add_f32_e32 v225, v225, v147
	v_add_f32_e32 v225, v225, v149
	v_add_f32_e32 v225, v225, v151
	v_add_f32_e32 v225, v225, v153
	v_add_f32_e32 v225, v225, v155
	v_add_f32_e32 v225, v225, v157
	v_add_f32_e32 v225, v225, v159
	v_add_f32_e32 v225, v225, v161
	v_fma_f32 v225, v225, v229, -v161
	v_cvt_pk_bf16_f32 v194, v194, v195
	v_cvt_pk_bf16_f32 v195, v196, v197
	v_cvt_pk_bf16_f32 v196, v198, v199
	v_cvt_pk_bf16_f32 v197, v200, v201
	global_store_dwordx4 v17, v[194:197], s[14:15]
	v_cvt_pk_bf16_f32 v202, v202, v203
	v_cvt_pk_bf16_f32 v203, v204, v205
	v_cvt_pk_bf16_f32 v204, v206, v207
	v_cvt_pk_bf16_f32 v205, v208, v209
	v_add_u32_e32 v13, 0x800, v17
	global_store_dwordx4 v13, v[202:205], s[14:15]
	v_cvt_pk_bf16_f32 v210, v210, v211
	v_cvt_pk_bf16_f32 v211, v212, v213
	v_cvt_pk_bf16_f32 v212, v214, v215
	v_cvt_pk_bf16_f32 v213, v216, v217
	v_add_u32_e32 v13, 0x1000, v17
	global_store_dwordx4 v13, v[210:213], s[14:15]
	v_cvt_pk_bf16_f32 v218, v218, v219
	v_cvt_pk_bf16_f32 v219, v220, v221
	v_cvt_pk_bf16_f32 v220, v222, v223
	v_cvt_pk_bf16_f32 v221, v224, v225
	v_add_u32_e32 v13, 0x1800, v17
	global_store_dwordx4 v13, v[218:221], s[14:15]
	s_branch .Lpc_conv

;     __device__ __forceinline__ const char* pb(const Unit& u) const { return (const char*)(Bt + ((size_t)u.pn * BM * ldb + (size_t)u.sub * b_sub)); }
; #define GRID_BAR() do { if (!MK_SPLIT) xcd_barrier(bar); } while (0)
; __global__ void __launch_bounds__(NTHR, 2) mk_fwd(Args args) {
;     ...
;         if (IN(pb + 1)) { poolconv_phase(F, F.conv_w + (size_t)l * 3 * 1024); scores_phase_mfma(F); GRID_BAR(); }
.LBB0_259:
	s_or_b64 exec, exec, s[2:3]
	s_cmp_eq_u32 s100, 2
	s_cbranch_scc0 .Lp2_cont
	s_mov_b32 s100, 3
	s_branch .LBB0_487
.Lp2_cont:
	s_mov_b64 s[2:3], -1
	s_branch .LBB0_261

;     __device__ __forceinline__ const char* pb(const Unit& u) const { return (const char*)(Bt + ((size_t)u.pn * BM * ldb + (size_t)u.sub * b_sub)); }
; __device__ __forceinline__ int lane_id() { int l; asm volatile("s_nop 4\n\tv_mbcnt_lo_u32_b32 %0, -1, 0\n\tv_mbcnt_hi_u32_b32 %0, -1, %0\n\ts_nop 4" : "=v"(l)); return l; }
; #define GRID_BAR() do { if (!MK_SPLIT) xcd_barrier(bar); } while (0)
; __device__ __forceinline__ void poolconv_phase(Frame& F, const float* conv_w_l) {
;     int tid = F.wave * 64 + lane_id(); asm volatile("" : "+v"(tid));
;     const int gt = F.vcu * NTHR + tid, NGT = F.G * NTHR;
;     for (int idx = gt; idx < M * 128; idx += NGT) {
;         const int grp = idx / (M * 32), rem = idx - grp * (M * 32), row = rem >> 5, c8 = grp * 256 + (rem & 31) * 8, t = row & (SEQ - 1);
;         if (grp == 0) pool_item<2>(F, row, t, c8); else if (grp == 1) pool_item<4>(F, row, t, c8); else if (grp == 2) pool_item<8>(F, row, t, c8); else pool_item<16>(F, row, t, c8);
;     }
;     for (int idx = gt; idx < M * 128; idx += NGT) {
; __global__ void __launch_bounds__(NTHR, 2) mk_fwd(Args args) {
;     ...
;         if (IN(pb + 1)) { poolconv_phase(F, F.conv_w + (size_t)l * 3 * 1024); scores_phase_mfma(F); GRID_BAR(); }
.LBB0_487:
	s_cmp_eq_u32 s100, 1
	s_cbranch_scc0 .Lp2_bar
	s_mov_b32 s100, 2
	s_movk_i32 s8, 0x1000
	s_mov_b32 s20, 0xff800000
	v_readlane_b32 s72, v255, 39
	v_readlane_b32 s73, v255, 40
	s_branch .Lp2_pool_start
